# 3 weight blocks per idle workgroup in the w_out and merge tail rounds; prologue keeps 928 of 4960 wq_single tasks
# baseline (speedup 1.0000x reference)
.LBB0_109:
	v_readlane_b32 s0, v251, 5
	v_readlane_b32 s6, v251, 11
	v_readlane_b32 s7, v251, 12
	s_add_u32 s0, s6, 0x10f00000
	v_writelane_b32 v252, s0, 12
	s_addc_u32 s0, s7, 0
	v_writelane_b32 v252, s0, 13
	s_add_u32 s0, s6, 0x3c90c0
	v_writelane_b32 v252, s0, 14
	s_addc_u32 s0, s7, 0
	v_writelane_b32 v252, s0, 15
	s_add_u32 s0, s6, 0x3ad0c0
	v_writelane_b32 v252, s0, 16
	s_addc_u32 s0, s7, 0
	v_writelane_b32 v252, s0, 17
	s_add_u32 s0, s6, 0x13800000
	v_writelane_b32 v252, s0, 18
	s_addc_u32 s0, s7, 0
	v_writelane_b32 v252, s0, 19
	s_add_u32 s0, s6, 0x33d0c0
	v_writelane_b32 v252, s0, 20
	s_addc_u32 s0, s7, 0
	v_writelane_b32 v252, s0, 21
	s_add_u32 s0, s6, 0x11700000
	v_writelane_b32 v252, s0, 22
	s_addc_u32 s0, s7, 0
	v_writelane_b32 v252, s0, 23
	s_add_u32 s0, s6, 0x3320c0
	v_mov_b32_e32 v0, 0x135f
	v_readlane_b32 s1, v251, 6
	v_writelane_b32 v252, s0, 24
	s_addc_u32 s0, s7, 0
	v_cmp_gt_i32_e32 vcc, s28, v0
	v_readlane_b32 s2, v251, 7
	v_readlane_b32 s3, v251, 8
	v_readlane_b32 s4, v251, 9
	v_readlane_b32 s5, v251, 10
	v_writelane_b32 v252, s0, 25
	s_and_b64 s[0:1], vcc, exec
	s_mov_b64 s[0:1], s[52:53]
	s_mov_b64 s[2:3], s[54:55]
	s_mov_b64 s[4:5], s[56:57]
	s_mov_b64 s[6:7], s[58:59]
	s_mov_b64 s[8:9], s[60:61]
	s_mov_b64 s[10:11], s[62:63]
	s_mov_b64 s[12:13], s[64:65]
	v_writelane_b32 v252, s0, 26
	s_waitcnt lgkmcnt(0)
	s_barrier
	v_writelane_b32 v252, s1, 27
	v_writelane_b32 v252, s2, 28
	v_writelane_b32 v252, s3, 29
	v_writelane_b32 v252, s4, 30
	v_writelane_b32 v252, s5, 31
	v_writelane_b32 v252, s6, 32
	v_writelane_b32 v252, s7, 33
	v_writelane_b32 v252, s8, 34
	v_writelane_b32 v252, s9, 35
	v_writelane_b32 v252, s10, 36
	v_writelane_b32 v252, s11, 37
	v_writelane_b32 v252, s12, 38
	v_writelane_b32 v252, s13, 39
	v_writelane_b32 v252, s14, 40
	v_writelane_b32 v252, s15, 41
	s_cbranch_scc1 .LBB0_253
	s_mov_b32 s98, s28
	v_readlane_b32 s100, v251, 24
	s_movk_i32 s99, 0x3a0
	s_mov_b32 s101, 0
	s_mov_b32 s0, 0xfffffa10
	s_cmp_lt_u32 s98, 0x1090
	s_cselect_b32 s0, 0xfffffa10, s0
	s_cmp_lt_u32 s98, 0xe50
	s_cselect_b32 s0, 0x510, s0
	s_cmp_lt_u32 s98, 0xe30
	s_cselect_b32 s0, 0x4b0, s0
	s_cmp_lt_u32 s98, 0xe20
	s_cselect_b32 s0, 0x4b0, s0
	s_cmp_lt_u32 s98, 0xd50
	s_cselect_b32 s0, 0xfffff410, s0
	s_cmp_lt_u32 s98, 0xca0
	s_cselect_b32 s0, 0x6a0, s0
	s_cmp_lt_u32 s98, 0xc80
	s_cselect_b32 s0, 0x580, s0
	s_cmp_lt_u32 s98, 0xba0
	s_cselect_b32 s0, 0xfffffcc0, s0
	s_cmp_lt_u32 s98, 0xb50
	s_cselect_b32 s0, 0xfffffcc0, s0
	s_cmp_lt_u32 s98, 0x8e0
	s_cselect_b32 s0, 0xfffffcc0, s0
	s_cmp_lt_u32 s98, 0x610
	s_cselect_b32 s0, 0xfffffcc0, s0
	s_cmp_lt_u32 s98, 0x4a0
	s_cselect_b32 s0, 0xe80, s0
	s_cmp_lt_u32 s98, 0x480
	s_cselect_b32 s0, 0xca0, s0
	s_cmp_lt_u32 s98, 0x3a0
	s_cselect_b32 s0, 0xbc0, s0
	s_cmp_lt_u32 s98, 0x1b0
	s_cselect_b32 s0, 0x1150, s0
	s_cmp_lt_u32 s98, 0x190
	s_cselect_b32 s0, 0xeb0, s0
	s_cmp_lt_u32 s98, 0xb0
	s_cselect_b32 s0, 0x0, s0
	s_add_i32 s28, s98, s0
	v_lshlrev_b32_e32 v0, 2, v50
	s_add_i32 s0, 0, 0x21000
	v_and_b32_e32 v37, 31, v50
	v_add_u32_e32 v39, s0, v0
	v_cmp_gt_i32_e64 s[0:1], 32, v50
	v_lshlrev_b32_e32 v1, 1, v50
	v_lshlrev_b32_e32 v42, 2, v37
	v_writelane_b32 v252, s0, 42
	v_ashrrev_i32_e32 v40, 3, v50
	v_and_b32_e32 v2, 0xffffffc0, v1
	v_add_u32_e32 v4, 0, v42
	v_writelane_b32 v252, s1, 43
	s_add_i32 s0, 0, 0x21800
	s_movk_i32 s2, 0x84
	v_and_b32_e32 v45, 7, v50
	v_add_u32_e32 v43, s0, v0
	v_add_u32_e32 v82, s0, v42
	v_mad_u64_u32 v[6:7], s[0:1], v2, s2, v[4:5]
	v_mul_lo_u32 v41, v40, s2
	v_lshlrev_b32_e32 v45, 4, v45
	v_add3_u32 v83, v41, v45, 0
	v_lshrrev_b32_e32 v45, 5, v50
	s_movk_i32 s0, 0x2100
	v_and_b32_e32 v35, 28, v0
	v_or_b32_e32 v0, 62, v1
	v_or_b32_e32 v1, 63, v1
	v_mul_lo_u32 v84, v45, s0
	v_mul_lo_u32 v0, v0, s2
	v_mul_lo_u32 v44, v1, s2
	v_or_b32_e32 v10, 2, v2
	v_or_b32_e32 v12, 4, v2
	v_or_b32_e32 v14, 6, v2
	v_or_b32_e32 v16, 8, v2
	v_or_b32_e32 v18, 10, v2
	v_or_b32_e32 v20, 12, v2
	v_or_b32_e32 v22, 14, v2
	v_or_b32_e32 v24, 16, v2
	v_or_b32_e32 v26, 18, v2
	v_or_b32_e32 v28, 20, v2
	v_or_b32_e32 v30, 22, v2
	v_or_b32_e32 v32, 24, v2
	v_or_b32_e32 v34, 26, v2
	v_or_b32_e32 v36, 28, v2
	v_or_b32_e32 v38, 30, v2
	v_ashrrev_i32_e32 v41, 31, v40
	v_or_b32_e32 v42, v84, v42
	v_ashrrev_i32_e32 v3, 31, v2
	v_mov_b32_e32 v8, v2
	v_mov_b32_e32 v1, v2
	v_mov_b32_e32 v5, v10
	v_mov_b32_e32 v7, v12
	v_mov_b32_e32 v9, v14
	v_mov_b32_e32 v11, v16
	v_mov_b32_e32 v13, v18
	v_mov_b32_e32 v15, v20
	v_mov_b32_e32 v17, v22
	v_mov_b32_e32 v19, v24
	v_mov_b32_e32 v21, v26
	v_mov_b32_e32 v23, v28
	v_mov_b32_e32 v25, v30
	v_mov_b32_e32 v27, v32
	v_mov_b32_e32 v29, v34
	v_mov_b32_e32 v31, v36
	v_mov_b32_e32 v33, v38
	v_lshlrev_b64 v[40:41], 2, v[40:41]
	v_add_u32_e32 v42, 0, v42
	v_mov_b32_e32 v45, 0
	v_add_u32_e32 v85, v4, v0
	v_add_u32_e32 v86, v4, v44
	s_branch .LBB0_112
.LBB0_111:
	s_or_b64 exec, exec, s[0:1]
	s_waitcnt lgkmcnt(0)
	s_barrier
	ds_read_b32 v0, v82
	ds_read_b32 v44, v85
	ds_read_b32 v58, v86
	s_mov_b32 s2, 0x42fe0000
	v_add_u32_e32 v57, 0x400, v6
	s_waitcnt lgkmcnt(2)
	v_div_scale_f32 v46, s[0:1], v0, v0, s2
	v_rcp_f32_e32 v47, v46
	v_readlane_b32 s0, v252, 46
	v_readlane_b32 s1, v252, 47
	v_add_u32_e32 v60, 0x800, v6
	v_fma_f32 v48, -v46, v47, 1.0
	v_fmac_f32_e32 v47, v48, v47
	v_div_scale_f32 v48, vcc, s2, v0, s2
	v_mul_f32_e32 v49, v48, v47
	v_fma_f32 v52, -v46, v49, v48
	v_fmac_f32_e32 v49, v52, v47
	v_fma_f32 v46, -v46, v49, v48
	v_div_fmas_f32 v46, v46, v47, v49
	ds_read2_b32 v[48:49], v6 offset1:33
	v_div_fixup_f32 v46, v46, v0, s2
	v_cmp_lt_f32_e32 vcc, 0, v0
	ds_read2_b32 v[52:53], v6 offset0:66 offset1:99
	v_readlane_b32 s28, v252, 44
	v_cndmask_b32_e32 v0, 0, v46, vcc
	s_waitcnt lgkmcnt(1)
	v_mul_f32_e32 v48, v48, v0
	v_rndne_f32_e32 v48, v48
	v_cvt_i32_f32_e32 v54, v48
	v_mul_f32_e32 v48, v0, v49
	v_rndne_f32_e32 v48, v48
	v_cvt_i32_f32_e32 v55, v48
	s_waitcnt lgkmcnt(0)
	v_mul_f32_e32 v48, v0, v52
	v_rndne_f32_e32 v48, v48
	v_cvt_i32_f32_sdwa v52, v48 dst_sel:WORD_1 dst_unused:UNUSED_PAD src0_sel:DWORD
	v_mul_f32_e32 v48, v0, v53
	v_or_b32_e32 v46, s33, v37
	v_rndne_f32_e32 v48, v48
	v_ashrrev_i32_e32 v47, 31, v46
	v_cvt_i32_f32_sdwa v53, v48 dst_sel:BYTE_3 dst_unused:UNUSED_PAD src0_sel:DWORD
	ds_read2_b32 v[48:49], v6 offset0:132 offset1:165
	v_lshlrev_b64 v[46:47], 10, v[46:47]
	v_lshl_add_u64 v[46:47], s[0:1], 0, v[46:47]
	v_lshlrev_b32_e32 v55, 8, v55
	s_mov_b32 s0, 0xc0c0500
	v_perm_b32 v54, v55, v54, s0
	v_and_b32_e32 v52, 0xff0000, v52
	v_or3_b32 v52, v54, v52, v53
	ds_read2_b32 v[54:55], v6 offset0:198 offset1:231
	s_waitcnt lgkmcnt(1)
	v_mul_f32_e32 v48, v0, v48
	v_rndne_f32_e32 v48, v48
	v_cvt_i32_f32_e32 v53, v48
	v_mul_f32_e32 v48, v0, v49
	v_rndne_f32_e32 v48, v48
	v_cvt_i32_f32_e32 v56, v48
	s_waitcnt lgkmcnt(0)
	v_mul_f32_e32 v48, v0, v54
	v_rndne_f32_e32 v48, v48
	v_cvt_i32_f32_sdwa v54, v48 dst_sel:WORD_1 dst_unused:UNUSED_PAD src0_sel:DWORD
	v_mul_f32_e32 v48, v0, v55
	v_rndne_f32_e32 v48, v48
	v_cvt_i32_f32_sdwa v55, v48 dst_sel:BYTE_3 dst_unused:UNUSED_PAD src0_sel:DWORD
	ds_read2_b32 v[48:49], v57 offset0:8 offset1:41
	v_lshlrev_b32_e32 v56, 8, v56
	v_perm_b32 v53, v56, v53, s0
	v_and_b32_e32 v54, 0xff0000, v54
	v_or3_b32 v53, v53, v54, v55
	ds_read2_b32 v[54:55], v57 offset0:74 offset1:107
	s_waitcnt lgkmcnt(1)
	v_mul_f32_e32 v48, v0, v48
	v_rndne_f32_e32 v48, v48
	v_cvt_i32_f32_e32 v56, v48
	v_mul_f32_e32 v48, v0, v49
	v_rndne_f32_e32 v48, v48
	v_cvt_i32_f32_e32 v59, v48
	s_waitcnt lgkmcnt(0)
	v_mul_f32_e32 v48, v0, v54
	v_rndne_f32_e32 v48, v48
	v_cvt_i32_f32_sdwa v54, v48 dst_sel:WORD_1 dst_unused:UNUSED_PAD src0_sel:DWORD
	v_mul_f32_e32 v48, v0, v55
	v_rndne_f32_e32 v48, v48
	v_cvt_i32_f32_sdwa v55, v48 dst_sel:BYTE_3 dst_unused:UNUSED_PAD src0_sel:DWORD
	ds_read2_b32 v[48:49], v57 offset0:140 offset1:173
	v_lshlrev_b32_e32 v59, 8, v59
	v_perm_b32 v56, v59, v56, s0
	v_and_b32_e32 v54, 0xff0000, v54
	v_or3_b32 v54, v56, v54, v55
	ds_read2_b32 v[56:57], v57 offset0:206 offset1:239
	s_waitcnt lgkmcnt(1)
	v_mul_f32_e32 v48, v0, v48
	v_mul_f32_e32 v49, v0, v49
	v_rndne_f32_e32 v48, v48
	v_rndne_f32_e32 v49, v49
	v_cvt_i32_f32_e32 v55, v48
	s_waitcnt lgkmcnt(0)
	v_mul_f32_e32 v48, v0, v56
	v_cvt_i32_f32_e32 v49, v49
	v_rndne_f32_e32 v48, v48
	v_cvt_i32_f32_sdwa v56, v48 dst_sel:WORD_1 dst_unused:UNUSED_PAD src0_sel:DWORD
	v_mul_f32_e32 v48, v0, v57
	v_rndne_f32_e32 v48, v48
	v_cvt_i32_f32_sdwa v57, v48 dst_sel:BYTE_3 dst_unused:UNUSED_PAD src0_sel:DWORD
	v_lshlrev_b32_e32 v59, 8, v49
	ds_read2_b32 v[48:49], v60 offset0:16 offset1:49
	v_perm_b32 v55, v59, v55, s0
	v_and_b32_e32 v56, 0xff0000, v56
	v_lshl_add_u64 v[46:47], v[46:47], 0, v[2:3]
	v_or3_b32 v55, v55, v56, v57
	global_store_dwordx4 v[46:47], v[52:55], off
	ds_read2_b32 v[52:53], v60 offset0:82 offset1:115
	s_waitcnt lgkmcnt(1)
	v_mul_f32_e32 v48, v0, v48
	v_rndne_f32_e32 v48, v48
	v_cvt_i32_f32_e32 v54, v48
	v_mul_f32_e32 v48, v0, v49
	v_rndne_f32_e32 v48, v48
	v_cvt_i32_f32_e32 v55, v48
	s_waitcnt lgkmcnt(0)
	v_mul_f32_e32 v48, v0, v52
	v_rndne_f32_e32 v48, v48
	v_cvt_i32_f32_sdwa v52, v48 dst_sel:WORD_1 dst_unused:UNUSED_PAD src0_sel:DWORD
	v_mul_f32_e32 v48, v0, v53
	v_rndne_f32_e32 v48, v48
	v_cvt_i32_f32_sdwa v53, v48 dst_sel:BYTE_3 dst_unused:UNUSED_PAD src0_sel:DWORD
	ds_read2_b32 v[48:49], v60 offset0:148 offset1:181
	v_lshlrev_b32_e32 v55, 8, v55
	v_perm_b32 v54, v55, v54, s0
	v_and_b32_e32 v52, 0xff0000, v52
	v_or3_b32 v52, v54, v52, v53
	ds_read2_b32 v[54:55], v60 offset0:214 offset1:247
	s_waitcnt lgkmcnt(1)
	v_mul_f32_e32 v48, v0, v48
	v_rndne_f32_e32 v48, v48
	v_cvt_i32_f32_e32 v53, v48
	v_mul_f32_e32 v48, v0, v49
	v_rndne_f32_e32 v48, v48
	v_cvt_i32_f32_e32 v56, v48
	s_waitcnt lgkmcnt(0)
	v_mul_f32_e32 v48, v0, v54
	v_rndne_f32_e32 v48, v48
	v_cvt_i32_f32_sdwa v54, v48 dst_sel:WORD_1 dst_unused:UNUSED_PAD src0_sel:DWORD
	v_mul_f32_e32 v48, v0, v55
	v_rndne_f32_e32 v48, v48
	v_add_u32_e32 v57, 0xc00, v6
	v_cvt_i32_f32_sdwa v55, v48 dst_sel:BYTE_3 dst_unused:UNUSED_PAD src0_sel:DWORD
	ds_read2_b32 v[48:49], v57 offset0:24 offset1:57
	v_lshlrev_b32_e32 v56, 8, v56
	v_perm_b32 v53, v56, v53, s0
	v_and_b32_e32 v54, 0xff0000, v54
	v_or3_b32 v53, v53, v54, v55
	ds_read2_b32 v[54:55], v57 offset0:90 offset1:123
	s_waitcnt lgkmcnt(1)
	v_mul_f32_e32 v48, v0, v48
	v_rndne_f32_e32 v48, v48
	v_cvt_i32_f32_e32 v56, v48
	v_mul_f32_e32 v48, v0, v49
	v_rndne_f32_e32 v48, v48
	v_cvt_i32_f32_e32 v59, v48
	s_waitcnt lgkmcnt(0)
	v_mul_f32_e32 v48, v0, v54
	v_rndne_f32_e32 v48, v48
	v_cvt_i32_f32_sdwa v54, v48 dst_sel:WORD_1 dst_unused:UNUSED_PAD src0_sel:DWORD
	v_mul_f32_e32 v48, v0, v55
	v_rndne_f32_e32 v48, v48
	v_cvt_i32_f32_sdwa v55, v48 dst_sel:BYTE_3 dst_unused:UNUSED_PAD src0_sel:DWORD
	ds_read2_b32 v[48:49], v57 offset0:156 offset1:189
	v_lshlrev_b32_e32 v59, 8, v59
	v_perm_b32 v56, v59, v56, s0
	v_and_b32_e32 v54, 0xff0000, v54
	v_or3_b32 v54, v56, v54, v55
	ds_read2_b32 v[56:57], v57 offset0:222 offset1:255
	s_waitcnt lgkmcnt(1)
	v_mul_f32_e32 v48, v0, v48
	v_mul_f32_e32 v49, v0, v49
	v_rndne_f32_e32 v48, v48
	v_rndne_f32_e32 v49, v49
	v_cvt_i32_f32_e32 v55, v48
	s_waitcnt lgkmcnt(0)
	v_mul_f32_e32 v48, v0, v56
	v_cvt_i32_f32_e32 v49, v49
	v_rndne_f32_e32 v48, v48
	v_cvt_i32_f32_sdwa v56, v48 dst_sel:WORD_1 dst_unused:UNUSED_PAD src0_sel:DWORD
	v_mul_f32_e32 v48, v0, v57
	v_rndne_f32_e32 v48, v48
	v_cvt_i32_f32_sdwa v57, v48 dst_sel:BYTE_3 dst_unused:UNUSED_PAD src0_sel:DWORD
	v_add_u32_e32 v60, 0x1000, v6
	v_lshlrev_b32_e32 v59, 8, v49
	ds_read2_b32 v[48:49], v60 offset0:32 offset1:65
	v_perm_b32 v55, v59, v55, s0
	v_and_b32_e32 v56, 0xff0000, v56
	v_or3_b32 v55, v55, v56, v57
	global_store_dwordx4 v[46:47], v[52:55], off offset:16
	ds_read2_b32 v[52:53], v60 offset0:98 offset1:131
	s_waitcnt lgkmcnt(1)
	v_mul_f32_e32 v48, v0, v48
	v_rndne_f32_e32 v48, v48
	v_cvt_i32_f32_e32 v54, v48
	v_mul_f32_e32 v48, v0, v49
	v_rndne_f32_e32 v48, v48
	v_cvt_i32_f32_e32 v55, v48
	s_waitcnt lgkmcnt(0)
	v_mul_f32_e32 v48, v0, v52
	v_rndne_f32_e32 v48, v48
	v_cvt_i32_f32_sdwa v52, v48 dst_sel:WORD_1 dst_unused:UNUSED_PAD src0_sel:DWORD
	v_mul_f32_e32 v48, v0, v53
	v_rndne_f32_e32 v48, v48
	v_cvt_i32_f32_sdwa v53, v48 dst_sel:BYTE_3 dst_unused:UNUSED_PAD src0_sel:DWORD
	ds_read2_b32 v[48:49], v60 offset0:164 offset1:197
	v_lshlrev_b32_e32 v55, 8, v55
	v_perm_b32 v54, v55, v54, s0
	v_and_b32_e32 v52, 0xff0000, v52
	v_or3_b32 v52, v54, v52, v53
	v_add_u32_e32 v53, 0x1200, v6
	ds_read2_b32 v[54:55], v53 offset0:102 offset1:135
	s_waitcnt lgkmcnt(1)
	v_mul_f32_e32 v48, v0, v48
	v_rndne_f32_e32 v48, v48
	v_cvt_i32_f32_e32 v53, v48
	v_mul_f32_e32 v48, v0, v49
	v_rndne_f32_e32 v48, v48
	v_cvt_i32_f32_e32 v56, v48
	s_waitcnt lgkmcnt(0)
	v_mul_f32_e32 v48, v0, v54
	v_rndne_f32_e32 v48, v48
	v_cvt_i32_f32_sdwa v54, v48 dst_sel:WORD_1 dst_unused:UNUSED_PAD src0_sel:DWORD
	v_mul_f32_e32 v48, v0, v55
	v_rndne_f32_e32 v48, v48
	v_add_u32_e32 v57, 0x1400, v6
	v_cvt_i32_f32_sdwa v55, v48 dst_sel:BYTE_3 dst_unused:UNUSED_PAD src0_sel:DWORD
	ds_read2_b32 v[48:49], v57 offset0:40 offset1:73
	v_lshlrev_b32_e32 v56, 8, v56
	v_perm_b32 v53, v56, v53, s0
	v_and_b32_e32 v54, 0xff0000, v54
	v_or3_b32 v53, v53, v54, v55
	ds_read2_b32 v[54:55], v57 offset0:106 offset1:139
	s_waitcnt lgkmcnt(1)
	v_mul_f32_e32 v48, v0, v48
	v_rndne_f32_e32 v48, v48
	v_cvt_i32_f32_e32 v56, v48
	v_mul_f32_e32 v48, v0, v49
	v_rndne_f32_e32 v48, v48
	v_cvt_i32_f32_e32 v59, v48
	s_waitcnt lgkmcnt(0)
	v_mul_f32_e32 v48, v0, v54
	v_rndne_f32_e32 v48, v48
	v_cvt_i32_f32_sdwa v54, v48 dst_sel:WORD_1 dst_unused:UNUSED_PAD src0_sel:DWORD
	v_mul_f32_e32 v48, v0, v55
	v_rndne_f32_e32 v48, v48
	v_cvt_i32_f32_sdwa v55, v48 dst_sel:BYTE_3 dst_unused:UNUSED_PAD src0_sel:DWORD
	ds_read2_b32 v[48:49], v57 offset0:172 offset1:205
	v_lshlrev_b32_e32 v57, 8, v59
	v_perm_b32 v56, v57, v56, s0
	v_and_b32_e32 v54, 0xff0000, v54
	v_or3_b32 v54, v56, v54, v55
	v_add_u32_e32 v55, 0x1600, v6
	ds_read2_b32 v[56:57], v55 offset0:110 offset1:143
	s_waitcnt lgkmcnt(1)
	v_mul_f32_e32 v48, v0, v48
	v_mul_f32_e32 v49, v0, v49
	v_rndne_f32_e32 v48, v48
	v_rndne_f32_e32 v49, v49
	v_cvt_i32_f32_e32 v55, v48
	s_waitcnt lgkmcnt(0)
	v_mul_f32_e32 v48, v0, v56
	v_cvt_i32_f32_e32 v49, v49
	v_rndne_f32_e32 v48, v48
	v_cvt_i32_f32_sdwa v56, v48 dst_sel:WORD_1 dst_unused:UNUSED_PAD src0_sel:DWORD
	v_mul_f32_e32 v48, v0, v57
	v_rndne_f32_e32 v48, v48
	v_cvt_i32_f32_sdwa v57, v48 dst_sel:BYTE_3 dst_unused:UNUSED_PAD src0_sel:DWORD
	v_add_u32_e32 v60, 0x1800, v6
	v_lshlrev_b32_e32 v59, 8, v49
	ds_read2_b32 v[48:49], v60 offset0:48 offset1:81
	v_perm_b32 v55, v59, v55, s0
	v_and_b32_e32 v56, 0xff0000, v56
	v_or3_b32 v55, v55, v56, v57
	global_store_dwordx4 v[46:47], v[52:55], off offset:32
	ds_read2_b32 v[52:53], v60 offset0:114 offset1:147
	s_waitcnt lgkmcnt(1)
	v_mul_f32_e32 v48, v0, v48
	v_rndne_f32_e32 v48, v48
	v_cvt_i32_f32_e32 v54, v48
	v_mul_f32_e32 v48, v0, v49
	v_rndne_f32_e32 v48, v48
	v_cvt_i32_f32_e32 v55, v48
	s_waitcnt lgkmcnt(0)
	v_mul_f32_e32 v48, v0, v52
	v_rndne_f32_e32 v48, v48
	v_cvt_i32_f32_sdwa v52, v48 dst_sel:WORD_1 dst_unused:UNUSED_PAD src0_sel:DWORD
	v_mul_f32_e32 v48, v0, v53
	v_rndne_f32_e32 v48, v48
	v_cvt_i32_f32_sdwa v53, v48 dst_sel:BYTE_3 dst_unused:UNUSED_PAD src0_sel:DWORD
	ds_read2_b32 v[48:49], v60 offset0:180 offset1:213
	v_lshlrev_b32_e32 v55, 8, v55
	v_perm_b32 v54, v55, v54, s0
	v_and_b32_e32 v52, 0xff0000, v52
	v_or3_b32 v52, v54, v52, v53
	v_add_u32_e32 v53, 0x1a00, v6
	ds_read2_b32 v[54:55], v53 offset0:118 offset1:151
	s_waitcnt lgkmcnt(1)
	v_mul_f32_e32 v48, v0, v48
	v_rndne_f32_e32 v48, v48
	v_cvt_i32_f32_e32 v53, v48
	v_mul_f32_e32 v48, v0, v49
	v_rndne_f32_e32 v48, v48
	v_cvt_i32_f32_e32 v56, v48
	s_waitcnt lgkmcnt(0)
	v_mul_f32_e32 v48, v0, v54
	v_rndne_f32_e32 v48, v48
	v_cvt_i32_f32_sdwa v54, v48 dst_sel:WORD_1 dst_unused:UNUSED_PAD src0_sel:DWORD
	v_mul_f32_e32 v48, v0, v55
	v_rndne_f32_e32 v48, v48
	v_add_u32_e32 v57, 0x1c00, v6
	v_cvt_i32_f32_sdwa v55, v48 dst_sel:BYTE_3 dst_unused:UNUSED_PAD src0_sel:DWORD
	ds_read2_b32 v[48:49], v57 offset0:56 offset1:89
	v_lshlrev_b32_e32 v56, 8, v56
	v_perm_b32 v53, v56, v53, s0
	v_and_b32_e32 v54, 0xff0000, v54
	v_or3_b32 v53, v53, v54, v55
	ds_read2_b32 v[54:55], v57 offset0:122 offset1:155
	s_waitcnt lgkmcnt(1)
	v_mul_f32_e32 v48, v0, v48
	v_rndne_f32_e32 v48, v48
	v_cvt_i32_f32_e32 v56, v48
	v_mul_f32_e32 v48, v0, v49
	v_rndne_f32_e32 v48, v48
	v_cvt_i32_f32_e32 v59, v48
	s_waitcnt lgkmcnt(0)
	v_mul_f32_e32 v48, v0, v54
	v_rndne_f32_e32 v48, v48
	v_cvt_i32_f32_sdwa v54, v48 dst_sel:WORD_1 dst_unused:UNUSED_PAD src0_sel:DWORD
	v_mul_f32_e32 v48, v0, v55
	v_rndne_f32_e32 v48, v48
	v_cvt_i32_f32_sdwa v55, v48 dst_sel:BYTE_3 dst_unused:UNUSED_PAD src0_sel:DWORD
	ds_read2_b32 v[48:49], v57 offset0:188 offset1:221
	v_mul_f32_e32 v44, v0, v44
	v_rndne_f32_e32 v44, v44
	v_cvt_i32_f32_sdwa v44, v44 dst_sel:WORD_1 dst_unused:UNUSED_PAD src0_sel:DWORD
	v_lshlrev_b32_e32 v57, 8, v59
	s_waitcnt lgkmcnt(0)
	v_mul_f32_e32 v49, v0, v49
	v_mul_f32_e32 v48, v0, v48
	v_rndne_f32_e32 v49, v49
	v_rndne_f32_e32 v48, v48
	v_cvt_i32_f32_e32 v49, v49
	v_cvt_i32_f32_e32 v48, v48
	v_mul_f32_e32 v0, v0, v58
	v_rndne_f32_e32 v0, v0
	v_cvt_i32_f32_sdwa v0, v0 dst_sel:BYTE_3 dst_unused:UNUSED_PAD src0_sel:DWORD
	v_lshlrev_b32_e32 v49, 8, v49
	v_perm_b32 v56, v57, v56, s0
	v_perm_b32 v48, v49, v48, s0
	s_add_i32 s98, s98, s100
	v_and_b32_e32 v54, 0xff0000, v54
	v_and_b32_e32 v44, 0xff0000, v44
	s_mov_b32 s0, 0xfffffa10
	s_cmp_lt_u32 s98, 0x1090
	s_cselect_b32 s0, 0xfffffa10, s0
	s_cmp_lt_u32 s98, 0xe50
	s_cselect_b32 s0, 0x510, s0
	s_cmp_lt_u32 s98, 0xe30
	s_cselect_b32 s0, 0x4b0, s0
	s_cmp_lt_u32 s98, 0xe20
	s_cselect_b32 s0, 0x4b0, s0
	s_cmp_lt_u32 s98, 0xd50
	s_cselect_b32 s0, 0xfffff410, s0
	s_cmp_lt_u32 s98, 0xca0
	s_cselect_b32 s0, 0x6a0, s0
	s_cmp_lt_u32 s98, 0xc80
	s_cselect_b32 s0, 0x580, s0
	s_cmp_lt_u32 s98, 0xba0
	s_cselect_b32 s0, 0xfffffcc0, s0
	s_cmp_lt_u32 s98, 0xb50
	s_cselect_b32 s0, 0xfffffcc0, s0
	s_cmp_lt_u32 s98, 0x8e0
	s_cselect_b32 s0, 0xfffffcc0, s0
	s_cmp_lt_u32 s98, 0x610
	s_cselect_b32 s0, 0xfffffcc0, s0
	s_cmp_lt_u32 s98, 0x4a0
	s_cselect_b32 s0, 0xe80, s0
	s_cmp_lt_u32 s98, 0x480
	s_cselect_b32 s0, 0xca0, s0
	s_cmp_lt_u32 s98, 0x3a0
	s_cselect_b32 s0, 0xbc0, s0
	s_cmp_lt_u32 s98, 0x1b0
	s_cselect_b32 s0, 0x1150, s0
	s_cmp_lt_u32 s98, 0x190
	s_cselect_b32 s0, 0xeb0, s0
	s_cmp_lt_u32 s98, 0xb0
	s_cselect_b32 s0, 0x0, s0
	s_add_i32 s28, s98, s0
	v_or3_b32 v54, v56, v54, v55
	v_or3_b32 v55, v48, v44, v0
	s_cmp_ge_u32 s98, s99
	global_store_dwordx4 v[46:47], v[52:55], off offset:48
	s_barrier
	s_cbranch_scc1 .LBB0_253

.LBB0_1028:
	v_readlane_b32 s98, v251, 3
	v_readlane_b32 s99, v255, 29
	s_cmp_lt_u32 s98, 48
	s_cbranch_scc1 .Lwqd_skip_M
	s_sub_i32 s98, s98, 48
	s_mov_b32 s100, 0
	s_mov_b32 s101, 0
	s_cmp_eq_u32 s99, 0
	s_cselect_b32 s100, 0x3a0, s100
	s_cselect_b32 s101, 0x610, s101
	s_cmp_eq_u32 s99, 1
	s_cselect_b32 s100, 0x8e0, s100
	s_cselect_b32 s101, 0xb50, s101
	s_cmp_eq_u32 s99, 2
	s_cselect_b32 s100, 0xe20, s100
	s_cselect_b32 s101, 0x1090, s101
	s_add_i32 s98, s98, s100
	s_mov_b32 s99, s101
	s_cmp_ge_u32 s98, s99
	s_cbranch_scc1 .Lwqd_skip_M
	s_movk_i32 s100, 208
	s_mov_b32 s101, 3
	v_writelane_b32 v117, s0, 0
	v_writelane_b32 v117, s1, 1
	v_writelane_b32 v117, s2, 2
	v_writelane_b32 v117, s3, 3
	v_writelane_b32 v117, s4, 4
	v_writelane_b32 v117, s5, 5
	v_writelane_b32 v117, s6, 6
	v_writelane_b32 v117, s7, 7
	v_writelane_b32 v117, s8, 8
	v_writelane_b32 v117, s9, 9
	v_writelane_b32 v117, s10, 10
	v_writelane_b32 v117, s11, 11
	v_writelane_b32 v117, s12, 12
	v_writelane_b32 v117, s13, 13
	v_writelane_b32 v117, s14, 14
	v_writelane_b32 v117, s15, 15
	v_writelane_b32 v117, s16, 16
	v_writelane_b32 v117, s17, 17
	v_writelane_b32 v117, s18, 18
	v_writelane_b32 v117, s19, 19
	v_writelane_b32 v117, s20, 20
	v_writelane_b32 v117, s21, 21
	v_writelane_b32 v117, s22, 22
	v_writelane_b32 v117, s23, 23
	v_writelane_b32 v117, s24, 24
	v_writelane_b32 v117, s25, 25
	v_writelane_b32 v117, s26, 26
	v_writelane_b32 v117, s27, 27
	v_writelane_b32 v117, s28, 28
	v_writelane_b32 v117, s29, 29
	v_writelane_b32 v117, s30, 30
	v_writelane_b32 v117, s31, 31
	v_writelane_b32 v117, s32, 32
	v_writelane_b32 v117, s33, 33
	v_writelane_b32 v117, s34, 34
	v_writelane_b32 v117, s35, 35
	v_writelane_b32 v117, s36, 36
	v_writelane_b32 v117, s37, 37
	v_writelane_b32 v117, s38, 38
	v_writelane_b32 v117, s39, 39
	v_writelane_b32 v117, s40, 40
	v_writelane_b32 v117, s41, 41
	v_writelane_b32 v117, s42, 42
	v_writelane_b32 v117, s43, 43
	v_writelane_b32 v117, s44, 44
	v_writelane_b32 v117, s45, 45
	v_writelane_b32 v117, s46, 46
	v_writelane_b32 v117, s47, 47
	v_writelane_b32 v117, s48, 48
	v_writelane_b32 v117, s49, 49
	v_writelane_b32 v117, s50, 50
	v_writelane_b32 v117, s51, 51
	v_writelane_b32 v117, s52, 52
	v_writelane_b32 v117, s53, 53
	v_writelane_b32 v117, s54, 54
	v_writelane_b32 v117, s55, 55
	v_writelane_b32 v117, s56, 56
	v_writelane_b32 v117, s57, 57
	v_writelane_b32 v117, s58, 58
	v_writelane_b32 v117, s59, 59
	v_writelane_b32 v117, s60, 60
	v_writelane_b32 v117, s61, 61
	v_writelane_b32 v117, s62, 62
	v_writelane_b32 v117, s63, 63
	v_writelane_b32 v118, s64, 0
	v_writelane_b32 v118, s65, 1
	v_writelane_b32 v118, s66, 2
	v_writelane_b32 v118, s67, 3
	v_writelane_b32 v118, s68, 4
	v_writelane_b32 v118, s69, 5
	v_writelane_b32 v118, s70, 6
	v_writelane_b32 v118, s71, 7
	v_writelane_b32 v118, s72, 8
	v_writelane_b32 v118, s73, 9
	v_writelane_b32 v118, s74, 10
	v_writelane_b32 v118, s75, 11
	v_writelane_b32 v118, s76, 12
	v_writelane_b32 v118, s77, 13
	v_writelane_b32 v118, s78, 14
	v_writelane_b32 v118, s79, 15
	v_writelane_b32 v118, s80, 16
	v_writelane_b32 v118, s81, 17
	v_writelane_b32 v118, s82, 18
	v_writelane_b32 v118, s83, 19
	v_writelane_b32 v118, s84, 20
	v_writelane_b32 v118, s85, 21
	v_writelane_b32 v118, s86, 22
	v_writelane_b32 v118, s87, 23
	v_writelane_b32 v118, s88, 24
	v_writelane_b32 v118, s89, 25
	v_writelane_b32 v118, s90, 26
	v_writelane_b32 v118, s91, 27
	v_writelane_b32 v118, s92, 28
	v_writelane_b32 v118, s93, 29
	v_writelane_b32 v118, s94, 30
	v_writelane_b32 v118, s95, 31
	v_writelane_b32 v118, s96, 32
	v_writelane_b32 v118, s97, 33
	v_mov_b32_e32 v100, v0
	v_mov_b32_e32 v101, v50
	v_mov_b32_e32 v102, v51
	v_mov_b32_e32 v103, v52
	v_mov_b32_e32 v104, v54
	v_mov_b32_e32 v105, v55
	v_mov_b32_e32 v106, v56
	v_mov_b32_e32 v107, v58
	v_mov_b32_e32 v108, v59
	v_mov_b32_e32 v109, v60
	v_mov_b32_e32 v110, v62
	v_mov_b32_e32 v111, v63
	v_mov_b32_e32 v112, v64
	v_mov_b32_e32 v113, v67
	v_mov_b32_e32 v114, v75
	v_mov_b32_e32 v115, v77
	s_branch .Lwqd_entry

.Lwqd_entry:
	v_mov_b32_e32 v50, v246
	v_mov_b32_e32 v5, 0
	v_readlane_b32 s52, v252, 26
	v_readlane_b32 s53, v252, 27
	s_mov_b32 s0, 0xfffffa10
	s_cmp_lt_u32 s98, 0x1090
	s_cselect_b32 s0, 0xfffffa10, s0
	s_cmp_lt_u32 s98, 0xe50
	s_cselect_b32 s0, 0x510, s0
	s_cmp_lt_u32 s98, 0xe30
	s_cselect_b32 s0, 0x4b0, s0
	s_cmp_lt_u32 s98, 0xe20
	s_cselect_b32 s0, 0x4b0, s0
	s_cmp_lt_u32 s98, 0xd50
	s_cselect_b32 s0, 0xfffff410, s0
	s_cmp_lt_u32 s98, 0xca0
	s_cselect_b32 s0, 0x6a0, s0
	s_cmp_lt_u32 s98, 0xc80
	s_cselect_b32 s0, 0x580, s0
	s_cmp_lt_u32 s98, 0xba0
	s_cselect_b32 s0, 0xfffffcc0, s0
	s_cmp_lt_u32 s98, 0xb50
	s_cselect_b32 s0, 0xfffffcc0, s0
	s_cmp_lt_u32 s98, 0x8e0
	s_cselect_b32 s0, 0xfffffcc0, s0
	s_cmp_lt_u32 s98, 0x610
	s_cselect_b32 s0, 0xfffffcc0, s0
	s_cmp_lt_u32 s98, 0x4a0
	s_cselect_b32 s0, 0xe80, s0
	s_cmp_lt_u32 s98, 0x480
	s_cselect_b32 s0, 0xca0, s0
	s_cmp_lt_u32 s98, 0x3a0
	s_cselect_b32 s0, 0xbc0, s0
	s_cmp_lt_u32 s98, 0x1b0
	s_cselect_b32 s0, 0x1150, s0
	s_cmp_lt_u32 s98, 0x190
	s_cselect_b32 s0, 0xeb0, s0
	s_cmp_lt_u32 s98, 0xb0
	s_cselect_b32 s0, 0x0, s0
	s_add_i32 s28, s98, s0
	v_lshlrev_b32_e32 v0, 2, v50
	s_add_i32 s0, 0, 0x21000
	v_and_b32_e32 v37, 31, v50
	v_add_u32_e32 v39, s0, v0
	v_cmp_gt_i32_e64 s[0:1], 32, v50
	v_lshlrev_b32_e32 v1, 1, v50
	v_lshlrev_b32_e32 v42, 2, v37
	v_writelane_b32 v116, s0, 0
	v_ashrrev_i32_e32 v40, 3, v50
	v_and_b32_e32 v2, 0xffffffc0, v1
	v_add_u32_e32 v4, 0, v42
	v_writelane_b32 v116, s1, 1
	s_add_i32 s0, 0, 0x21800
	s_movk_i32 s2, 0x84
	v_and_b32_e32 v45, 7, v50
	v_add_u32_e32 v43, s0, v0
	v_add_u32_e32 v82, s0, v42
	v_mad_u64_u32 v[6:7], s[0:1], v2, s2, v[4:5]
	v_mul_lo_u32 v41, v40, s2
	v_lshlrev_b32_e32 v45, 4, v45
	v_add3_u32 v83, v41, v45, 0
	v_lshrrev_b32_e32 v45, 5, v50
	s_movk_i32 s0, 0x2100
	v_and_b32_e32 v35, 28, v0
	v_or_b32_e32 v0, 62, v1
	v_or_b32_e32 v1, 63, v1
	v_mul_lo_u32 v84, v45, s0
	v_mul_lo_u32 v0, v0, s2
	v_mul_lo_u32 v44, v1, s2
	v_or_b32_e32 v10, 2, v2
	v_or_b32_e32 v12, 4, v2
	v_or_b32_e32 v14, 6, v2
	v_or_b32_e32 v16, 8, v2
	v_or_b32_e32 v18, 10, v2
	v_or_b32_e32 v20, 12, v2
	v_or_b32_e32 v22, 14, v2
	v_or_b32_e32 v24, 16, v2
	v_or_b32_e32 v26, 18, v2
	v_or_b32_e32 v28, 20, v2
	v_or_b32_e32 v30, 22, v2
	v_or_b32_e32 v32, 24, v2
	v_or_b32_e32 v34, 26, v2
	v_or_b32_e32 v36, 28, v2
	v_or_b32_e32 v38, 30, v2
	v_ashrrev_i32_e32 v41, 31, v40
	v_or_b32_e32 v42, v84, v42
	v_ashrrev_i32_e32 v3, 31, v2
	v_mov_b32_e32 v8, v2
	v_mov_b32_e32 v1, v2
	v_mov_b32_e32 v5, v10
	v_mov_b32_e32 v7, v12
	v_mov_b32_e32 v9, v14
	v_mov_b32_e32 v11, v16
	v_mov_b32_e32 v13, v18
	v_mov_b32_e32 v15, v20
	v_mov_b32_e32 v17, v22
	v_mov_b32_e32 v19, v24
	v_mov_b32_e32 v21, v26
	v_mov_b32_e32 v23, v28
	v_mov_b32_e32 v25, v30
	v_mov_b32_e32 v27, v32
	v_mov_b32_e32 v29, v34
	v_mov_b32_e32 v31, v36
	v_mov_b32_e32 v33, v38
	v_lshlrev_b64 v[40:41], 2, v[40:41]
	v_add_u32_e32 v42, 0, v42
	v_mov_b32_e32 v45, 0
	v_add_u32_e32 v85, v4, v0
	v_add_u32_e32 v86, v4, v44
	s_branch .Lwqd_112
.Lwqd_111:
	s_or_b64 exec, exec, s[0:1]
	s_waitcnt lgkmcnt(0)
	s_barrier
	ds_read_b32 v0, v82
	ds_read_b32 v44, v85
	ds_read_b32 v58, v86
	s_mov_b32 s2, 0x42fe0000
	v_add_u32_e32 v57, 0x400, v6
	s_waitcnt lgkmcnt(2)
	v_div_scale_f32 v46, s[0:1], v0, v0, s2
	v_rcp_f32_e32 v47, v46
	v_readlane_b32 s0, v116, 4
	v_readlane_b32 s1, v116, 5
	v_add_u32_e32 v60, 0x800, v6
	v_fma_f32 v48, -v46, v47, 1.0
	v_fmac_f32_e32 v47, v48, v47
	v_div_scale_f32 v48, vcc, s2, v0, s2
	v_mul_f32_e32 v49, v48, v47
	v_fma_f32 v52, -v46, v49, v48
	v_fmac_f32_e32 v49, v52, v47
	v_fma_f32 v46, -v46, v49, v48
	v_div_fmas_f32 v46, v46, v47, v49
	ds_read2_b32 v[48:49], v6 offset1:33
	v_div_fixup_f32 v46, v46, v0, s2
	v_cmp_lt_f32_e32 vcc, 0, v0
	ds_read2_b32 v[52:53], v6 offset0:66 offset1:99
	v_readlane_b32 s28, v116, 2
	v_cndmask_b32_e32 v0, 0, v46, vcc
	s_waitcnt lgkmcnt(1)
	v_mul_f32_e32 v48, v48, v0
	v_rndne_f32_e32 v48, v48
	v_cvt_i32_f32_e32 v54, v48
	v_mul_f32_e32 v48, v0, v49
	v_rndne_f32_e32 v48, v48
	v_cvt_i32_f32_e32 v55, v48
	s_waitcnt lgkmcnt(0)
	v_mul_f32_e32 v48, v0, v52
	v_rndne_f32_e32 v48, v48
	v_cvt_i32_f32_sdwa v52, v48 dst_sel:WORD_1 dst_unused:UNUSED_PAD src0_sel:DWORD
	v_mul_f32_e32 v48, v0, v53
	v_or_b32_e32 v46, s33, v37
	v_rndne_f32_e32 v48, v48
	v_ashrrev_i32_e32 v47, 31, v46
	v_cvt_i32_f32_sdwa v53, v48 dst_sel:BYTE_3 dst_unused:UNUSED_PAD src0_sel:DWORD
	ds_read2_b32 v[48:49], v6 offset0:132 offset1:165
	v_lshlrev_b64 v[46:47], 10, v[46:47]
	v_lshl_add_u64 v[46:47], s[0:1], 0, v[46:47]
	v_lshlrev_b32_e32 v55, 8, v55
	s_mov_b32 s0, 0xc0c0500
	v_perm_b32 v54, v55, v54, s0
	v_and_b32_e32 v52, 0xff0000, v52
	v_or3_b32 v52, v54, v52, v53
	ds_read2_b32 v[54:55], v6 offset0:198 offset1:231
	s_waitcnt lgkmcnt(1)
	v_mul_f32_e32 v48, v0, v48
	v_rndne_f32_e32 v48, v48
	v_cvt_i32_f32_e32 v53, v48
	v_mul_f32_e32 v48, v0, v49
	v_rndne_f32_e32 v48, v48
	v_cvt_i32_f32_e32 v56, v48
	s_waitcnt lgkmcnt(0)
	v_mul_f32_e32 v48, v0, v54
	v_rndne_f32_e32 v48, v48
	v_cvt_i32_f32_sdwa v54, v48 dst_sel:WORD_1 dst_unused:UNUSED_PAD src0_sel:DWORD
	v_mul_f32_e32 v48, v0, v55
	v_rndne_f32_e32 v48, v48
	v_cvt_i32_f32_sdwa v55, v48 dst_sel:BYTE_3 dst_unused:UNUSED_PAD src0_sel:DWORD
	ds_read2_b32 v[48:49], v57 offset0:8 offset1:41
	v_lshlrev_b32_e32 v56, 8, v56
	v_perm_b32 v53, v56, v53, s0
	v_and_b32_e32 v54, 0xff0000, v54
	v_or3_b32 v53, v53, v54, v55
	ds_read2_b32 v[54:55], v57 offset0:74 offset1:107
	s_waitcnt lgkmcnt(1)
	v_mul_f32_e32 v48, v0, v48
	v_rndne_f32_e32 v48, v48
	v_cvt_i32_f32_e32 v56, v48
	v_mul_f32_e32 v48, v0, v49
	v_rndne_f32_e32 v48, v48
	v_cvt_i32_f32_e32 v59, v48
	s_waitcnt lgkmcnt(0)
	v_mul_f32_e32 v48, v0, v54
	v_rndne_f32_e32 v48, v48
	v_cvt_i32_f32_sdwa v54, v48 dst_sel:WORD_1 dst_unused:UNUSED_PAD src0_sel:DWORD
	v_mul_f32_e32 v48, v0, v55
	v_rndne_f32_e32 v48, v48
	v_cvt_i32_f32_sdwa v55, v48 dst_sel:BYTE_3 dst_unused:UNUSED_PAD src0_sel:DWORD
	ds_read2_b32 v[48:49], v57 offset0:140 offset1:173
	v_lshlrev_b32_e32 v59, 8, v59
	v_perm_b32 v56, v59, v56, s0
	v_and_b32_e32 v54, 0xff0000, v54
	v_or3_b32 v54, v56, v54, v55
	ds_read2_b32 v[56:57], v57 offset0:206 offset1:239
	s_waitcnt lgkmcnt(1)
	v_mul_f32_e32 v48, v0, v48
	v_mul_f32_e32 v49, v0, v49
	v_rndne_f32_e32 v48, v48
	v_rndne_f32_e32 v49, v49
	v_cvt_i32_f32_e32 v55, v48
	s_waitcnt lgkmcnt(0)
	v_mul_f32_e32 v48, v0, v56
	v_cvt_i32_f32_e32 v49, v49
	v_rndne_f32_e32 v48, v48
	v_cvt_i32_f32_sdwa v56, v48 dst_sel:WORD_1 dst_unused:UNUSED_PAD src0_sel:DWORD
	v_mul_f32_e32 v48, v0, v57
	v_rndne_f32_e32 v48, v48
	v_cvt_i32_f32_sdwa v57, v48 dst_sel:BYTE_3 dst_unused:UNUSED_PAD src0_sel:DWORD
	v_lshlrev_b32_e32 v59, 8, v49
	ds_read2_b32 v[48:49], v60 offset0:16 offset1:49
	v_perm_b32 v55, v59, v55, s0
	v_and_b32_e32 v56, 0xff0000, v56
	v_lshl_add_u64 v[46:47], v[46:47], 0, v[2:3]
	v_or3_b32 v55, v55, v56, v57
	global_store_dwordx4 v[46:47], v[52:55], off
	ds_read2_b32 v[52:53], v60 offset0:82 offset1:115
	s_waitcnt lgkmcnt(1)
	v_mul_f32_e32 v48, v0, v48
	v_rndne_f32_e32 v48, v48
	v_cvt_i32_f32_e32 v54, v48
	v_mul_f32_e32 v48, v0, v49
	v_rndne_f32_e32 v48, v48
	v_cvt_i32_f32_e32 v55, v48
	s_waitcnt lgkmcnt(0)
	v_mul_f32_e32 v48, v0, v52
	v_rndne_f32_e32 v48, v48
	v_cvt_i32_f32_sdwa v52, v48 dst_sel:WORD_1 dst_unused:UNUSED_PAD src0_sel:DWORD
	v_mul_f32_e32 v48, v0, v53
	v_rndne_f32_e32 v48, v48
	v_cvt_i32_f32_sdwa v53, v48 dst_sel:BYTE_3 dst_unused:UNUSED_PAD src0_sel:DWORD
	ds_read2_b32 v[48:49], v60 offset0:148 offset1:181
	v_lshlrev_b32_e32 v55, 8, v55
	v_perm_b32 v54, v55, v54, s0
	v_and_b32_e32 v52, 0xff0000, v52
	v_or3_b32 v52, v54, v52, v53
	ds_read2_b32 v[54:55], v60 offset0:214 offset1:247
	s_waitcnt lgkmcnt(1)
	v_mul_f32_e32 v48, v0, v48
	v_rndne_f32_e32 v48, v48
	v_cvt_i32_f32_e32 v53, v48
	v_mul_f32_e32 v48, v0, v49
	v_rndne_f32_e32 v48, v48
	v_cvt_i32_f32_e32 v56, v48
	s_waitcnt lgkmcnt(0)
	v_mul_f32_e32 v48, v0, v54
	v_rndne_f32_e32 v48, v48
	v_cvt_i32_f32_sdwa v54, v48 dst_sel:WORD_1 dst_unused:UNUSED_PAD src0_sel:DWORD
	v_mul_f32_e32 v48, v0, v55
	v_rndne_f32_e32 v48, v48
	v_add_u32_e32 v57, 0xc00, v6
	v_cvt_i32_f32_sdwa v55, v48 dst_sel:BYTE_3 dst_unused:UNUSED_PAD src0_sel:DWORD
	ds_read2_b32 v[48:49], v57 offset0:24 offset1:57
	v_lshlrev_b32_e32 v56, 8, v56
	v_perm_b32 v53, v56, v53, s0
	v_and_b32_e32 v54, 0xff0000, v54
	v_or3_b32 v53, v53, v54, v55
	ds_read2_b32 v[54:55], v57 offset0:90 offset1:123
	s_waitcnt lgkmcnt(1)
	v_mul_f32_e32 v48, v0, v48
	v_rndne_f32_e32 v48, v48
	v_cvt_i32_f32_e32 v56, v48
	v_mul_f32_e32 v48, v0, v49
	v_rndne_f32_e32 v48, v48
	v_cvt_i32_f32_e32 v59, v48
	s_waitcnt lgkmcnt(0)
	v_mul_f32_e32 v48, v0, v54
	v_rndne_f32_e32 v48, v48
	v_cvt_i32_f32_sdwa v54, v48 dst_sel:WORD_1 dst_unused:UNUSED_PAD src0_sel:DWORD
	v_mul_f32_e32 v48, v0, v55
	v_rndne_f32_e32 v48, v48
	v_cvt_i32_f32_sdwa v55, v48 dst_sel:BYTE_3 dst_unused:UNUSED_PAD src0_sel:DWORD
	ds_read2_b32 v[48:49], v57 offset0:156 offset1:189
	v_lshlrev_b32_e32 v59, 8, v59
	v_perm_b32 v56, v59, v56, s0
	v_and_b32_e32 v54, 0xff0000, v54
	v_or3_b32 v54, v56, v54, v55
	ds_read2_b32 v[56:57], v57 offset0:222 offset1:255
	s_waitcnt lgkmcnt(1)
	v_mul_f32_e32 v48, v0, v48
	v_mul_f32_e32 v49, v0, v49
	v_rndne_f32_e32 v48, v48
	v_rndne_f32_e32 v49, v49
	v_cvt_i32_f32_e32 v55, v48
	s_waitcnt lgkmcnt(0)
	v_mul_f32_e32 v48, v0, v56
	v_cvt_i32_f32_e32 v49, v49
	v_rndne_f32_e32 v48, v48
	v_cvt_i32_f32_sdwa v56, v48 dst_sel:WORD_1 dst_unused:UNUSED_PAD src0_sel:DWORD
	v_mul_f32_e32 v48, v0, v57
	v_rndne_f32_e32 v48, v48
	v_cvt_i32_f32_sdwa v57, v48 dst_sel:BYTE_3 dst_unused:UNUSED_PAD src0_sel:DWORD
	v_add_u32_e32 v60, 0x1000, v6
	v_lshlrev_b32_e32 v59, 8, v49
	ds_read2_b32 v[48:49], v60 offset0:32 offset1:65
	v_perm_b32 v55, v59, v55, s0
	v_and_b32_e32 v56, 0xff0000, v56
	v_or3_b32 v55, v55, v56, v57
	global_store_dwordx4 v[46:47], v[52:55], off offset:16
	ds_read2_b32 v[52:53], v60 offset0:98 offset1:131
	s_waitcnt lgkmcnt(1)
	v_mul_f32_e32 v48, v0, v48
	v_rndne_f32_e32 v48, v48
	v_cvt_i32_f32_e32 v54, v48
	v_mul_f32_e32 v48, v0, v49
	v_rndne_f32_e32 v48, v48
	v_cvt_i32_f32_e32 v55, v48
	s_waitcnt lgkmcnt(0)
	v_mul_f32_e32 v48, v0, v52
	v_rndne_f32_e32 v48, v48
	v_cvt_i32_f32_sdwa v52, v48 dst_sel:WORD_1 dst_unused:UNUSED_PAD src0_sel:DWORD
	v_mul_f32_e32 v48, v0, v53
	v_rndne_f32_e32 v48, v48
	v_cvt_i32_f32_sdwa v53, v48 dst_sel:BYTE_3 dst_unused:UNUSED_PAD src0_sel:DWORD
	ds_read2_b32 v[48:49], v60 offset0:164 offset1:197
	v_lshlrev_b32_e32 v55, 8, v55
	v_perm_b32 v54, v55, v54, s0
	v_and_b32_e32 v52, 0xff0000, v52
	v_or3_b32 v52, v54, v52, v53
	v_add_u32_e32 v53, 0x1200, v6
	ds_read2_b32 v[54:55], v53 offset0:102 offset1:135
	s_waitcnt lgkmcnt(1)
	v_mul_f32_e32 v48, v0, v48
	v_rndne_f32_e32 v48, v48
	v_cvt_i32_f32_e32 v53, v48
	v_mul_f32_e32 v48, v0, v49
	v_rndne_f32_e32 v48, v48
	v_cvt_i32_f32_e32 v56, v48
	s_waitcnt lgkmcnt(0)
	v_mul_f32_e32 v48, v0, v54
	v_rndne_f32_e32 v48, v48
	v_cvt_i32_f32_sdwa v54, v48 dst_sel:WORD_1 dst_unused:UNUSED_PAD src0_sel:DWORD
	v_mul_f32_e32 v48, v0, v55
	v_rndne_f32_e32 v48, v48
	v_add_u32_e32 v57, 0x1400, v6
	v_cvt_i32_f32_sdwa v55, v48 dst_sel:BYTE_3 dst_unused:UNUSED_PAD src0_sel:DWORD
	ds_read2_b32 v[48:49], v57 offset0:40 offset1:73
	v_lshlrev_b32_e32 v56, 8, v56
	v_perm_b32 v53, v56, v53, s0
	v_and_b32_e32 v54, 0xff0000, v54
	v_or3_b32 v53, v53, v54, v55
	ds_read2_b32 v[54:55], v57 offset0:106 offset1:139
	s_waitcnt lgkmcnt(1)
	v_mul_f32_e32 v48, v0, v48
	v_rndne_f32_e32 v48, v48
	v_cvt_i32_f32_e32 v56, v48
	v_mul_f32_e32 v48, v0, v49
	v_rndne_f32_e32 v48, v48
	v_cvt_i32_f32_e32 v59, v48
	s_waitcnt lgkmcnt(0)
	v_mul_f32_e32 v48, v0, v54
	v_rndne_f32_e32 v48, v48
	v_cvt_i32_f32_sdwa v54, v48 dst_sel:WORD_1 dst_unused:UNUSED_PAD src0_sel:DWORD
	v_mul_f32_e32 v48, v0, v55
	v_rndne_f32_e32 v48, v48
	v_cvt_i32_f32_sdwa v55, v48 dst_sel:BYTE_3 dst_unused:UNUSED_PAD src0_sel:DWORD
	ds_read2_b32 v[48:49], v57 offset0:172 offset1:205
	v_lshlrev_b32_e32 v57, 8, v59
	v_perm_b32 v56, v57, v56, s0
	v_and_b32_e32 v54, 0xff0000, v54
	v_or3_b32 v54, v56, v54, v55
	v_add_u32_e32 v55, 0x1600, v6
	ds_read2_b32 v[56:57], v55 offset0:110 offset1:143
	s_waitcnt lgkmcnt(1)
	v_mul_f32_e32 v48, v0, v48
	v_mul_f32_e32 v49, v0, v49
	v_rndne_f32_e32 v48, v48
	v_rndne_f32_e32 v49, v49
	v_cvt_i32_f32_e32 v55, v48
	s_waitcnt lgkmcnt(0)
	v_mul_f32_e32 v48, v0, v56
	v_cvt_i32_f32_e32 v49, v49
	v_rndne_f32_e32 v48, v48
	v_cvt_i32_f32_sdwa v56, v48 dst_sel:WORD_1 dst_unused:UNUSED_PAD src0_sel:DWORD
	v_mul_f32_e32 v48, v0, v57
	v_rndne_f32_e32 v48, v48
	v_cvt_i32_f32_sdwa v57, v48 dst_sel:BYTE_3 dst_unused:UNUSED_PAD src0_sel:DWORD
	v_add_u32_e32 v60, 0x1800, v6
	v_lshlrev_b32_e32 v59, 8, v49
	ds_read2_b32 v[48:49], v60 offset0:48 offset1:81
	v_perm_b32 v55, v59, v55, s0
	v_and_b32_e32 v56, 0xff0000, v56
	v_or3_b32 v55, v55, v56, v57
	global_store_dwordx4 v[46:47], v[52:55], off offset:32
	ds_read2_b32 v[52:53], v60 offset0:114 offset1:147
	s_waitcnt lgkmcnt(1)
	v_mul_f32_e32 v48, v0, v48
	v_rndne_f32_e32 v48, v48
	v_cvt_i32_f32_e32 v54, v48
	v_mul_f32_e32 v48, v0, v49
	v_rndne_f32_e32 v48, v48
	v_cvt_i32_f32_e32 v55, v48
	s_waitcnt lgkmcnt(0)
	v_mul_f32_e32 v48, v0, v52
	v_rndne_f32_e32 v48, v48
	v_cvt_i32_f32_sdwa v52, v48 dst_sel:WORD_1 dst_unused:UNUSED_PAD src0_sel:DWORD
	v_mul_f32_e32 v48, v0, v53
	v_rndne_f32_e32 v48, v48
	v_cvt_i32_f32_sdwa v53, v48 dst_sel:BYTE_3 dst_unused:UNUSED_PAD src0_sel:DWORD
	ds_read2_b32 v[48:49], v60 offset0:180 offset1:213
	v_lshlrev_b32_e32 v55, 8, v55
	v_perm_b32 v54, v55, v54, s0
	v_and_b32_e32 v52, 0xff0000, v52
	v_or3_b32 v52, v54, v52, v53
	v_add_u32_e32 v53, 0x1a00, v6
	ds_read2_b32 v[54:55], v53 offset0:118 offset1:151
	s_waitcnt lgkmcnt(1)
	v_mul_f32_e32 v48, v0, v48
	v_rndne_f32_e32 v48, v48
	v_cvt_i32_f32_e32 v53, v48
	v_mul_f32_e32 v48, v0, v49
	v_rndne_f32_e32 v48, v48
	v_cvt_i32_f32_e32 v56, v48
	s_waitcnt lgkmcnt(0)
	v_mul_f32_e32 v48, v0, v54
	v_rndne_f32_e32 v48, v48
	v_cvt_i32_f32_sdwa v54, v48 dst_sel:WORD_1 dst_unused:UNUSED_PAD src0_sel:DWORD
	v_mul_f32_e32 v48, v0, v55
	v_rndne_f32_e32 v48, v48
	v_add_u32_e32 v57, 0x1c00, v6
	v_cvt_i32_f32_sdwa v55, v48 dst_sel:BYTE_3 dst_unused:UNUSED_PAD src0_sel:DWORD
	ds_read2_b32 v[48:49], v57 offset0:56 offset1:89
	v_lshlrev_b32_e32 v56, 8, v56
	v_perm_b32 v53, v56, v53, s0
	v_and_b32_e32 v54, 0xff0000, v54
	v_or3_b32 v53, v53, v54, v55
	ds_read2_b32 v[54:55], v57 offset0:122 offset1:155
	s_waitcnt lgkmcnt(1)
	v_mul_f32_e32 v48, v0, v48
	v_rndne_f32_e32 v48, v48
	v_cvt_i32_f32_e32 v56, v48
	v_mul_f32_e32 v48, v0, v49
	v_rndne_f32_e32 v48, v48
	v_cvt_i32_f32_e32 v59, v48
	s_waitcnt lgkmcnt(0)
	v_mul_f32_e32 v48, v0, v54
	v_rndne_f32_e32 v48, v48
	v_cvt_i32_f32_sdwa v54, v48 dst_sel:WORD_1 dst_unused:UNUSED_PAD src0_sel:DWORD
	v_mul_f32_e32 v48, v0, v55
	v_rndne_f32_e32 v48, v48
	v_cvt_i32_f32_sdwa v55, v48 dst_sel:BYTE_3 dst_unused:UNUSED_PAD src0_sel:DWORD
	ds_read2_b32 v[48:49], v57 offset0:188 offset1:221
	v_mul_f32_e32 v44, v0, v44
	v_rndne_f32_e32 v44, v44
	v_cvt_i32_f32_sdwa v44, v44 dst_sel:WORD_1 dst_unused:UNUSED_PAD src0_sel:DWORD
	v_lshlrev_b32_e32 v57, 8, v59
	s_waitcnt lgkmcnt(0)
	v_mul_f32_e32 v49, v0, v49
	v_mul_f32_e32 v48, v0, v48
	v_rndne_f32_e32 v49, v49
	v_rndne_f32_e32 v48, v48
	v_cvt_i32_f32_e32 v49, v49
	v_cvt_i32_f32_e32 v48, v48
	v_mul_f32_e32 v0, v0, v58
	v_rndne_f32_e32 v0, v0
	v_cvt_i32_f32_sdwa v0, v0 dst_sel:BYTE_3 dst_unused:UNUSED_PAD src0_sel:DWORD
	v_lshlrev_b32_e32 v49, 8, v49
	v_perm_b32 v56, v57, v56, s0
	v_perm_b32 v48, v49, v48, s0
	s_add_i32 s98, s98, s100
	v_and_b32_e32 v54, 0xff0000, v54
	v_and_b32_e32 v44, 0xff0000, v44
	s_mov_b32 s0, 0xfffffa10
	s_cmp_lt_u32 s98, 0x1090
	s_cselect_b32 s0, 0xfffffa10, s0
	s_cmp_lt_u32 s98, 0xe50
	s_cselect_b32 s0, 0x510, s0
	s_cmp_lt_u32 s98, 0xe30
	s_cselect_b32 s0, 0x4b0, s0
	s_cmp_lt_u32 s98, 0xe20
	s_cselect_b32 s0, 0x4b0, s0
	s_cmp_lt_u32 s98, 0xd50
	s_cselect_b32 s0, 0xfffff410, s0
	s_cmp_lt_u32 s98, 0xca0
	s_cselect_b32 s0, 0x6a0, s0
	s_cmp_lt_u32 s98, 0xc80
	s_cselect_b32 s0, 0x580, s0
	s_cmp_lt_u32 s98, 0xba0
	s_cselect_b32 s0, 0xfffffcc0, s0
	s_cmp_lt_u32 s98, 0xb50
	s_cselect_b32 s0, 0xfffffcc0, s0
	s_cmp_lt_u32 s98, 0x8e0
	s_cselect_b32 s0, 0xfffffcc0, s0
	s_cmp_lt_u32 s98, 0x610
	s_cselect_b32 s0, 0xfffffcc0, s0
	s_cmp_lt_u32 s98, 0x4a0
	s_cselect_b32 s0, 0xe80, s0
	s_cmp_lt_u32 s98, 0x480
	s_cselect_b32 s0, 0xca0, s0
	s_cmp_lt_u32 s98, 0x3a0
	s_cselect_b32 s0, 0xbc0, s0
	s_cmp_lt_u32 s98, 0x1b0
	s_cselect_b32 s0, 0x1150, s0
	s_cmp_lt_u32 s98, 0x190
	s_cselect_b32 s0, 0xeb0, s0
	s_cmp_lt_u32 s98, 0xb0
	s_cselect_b32 s0, 0x0, s0
	s_add_i32 s28, s98, s0
	v_or3_b32 v54, v56, v54, v55
	v_or3_b32 v55, v48, v44, v0
	s_cmp_ge_u32 s98, s99
	global_store_dwordx4 v[46:47], v[52:55], off offset:48
	s_barrier
	s_cbranch_scc1 .Lwqd_exit

.Lwqd_exit:
	s_mov_b64 exec, -1
	s_cmp_eq_u32 s101, 1
	s_cbranch_scc1 .Lwqd_ret_A
	s_cmp_eq_u32 s101, 3
	s_cbranch_scc1 .Lwqd_ret_M
	s_endpgm

.LBB0_1159:
	v_readlane_b32 s98, v251, 3
	v_readlane_b32 s99, v255, 29
	s_cmp_lt_u32 s98, 16
	s_cbranch_scc1 .Lwqd_skip_A
	s_sub_i32 s98, s98, 16
	s_mov_b32 s100, 0
	s_mov_b32 s101, 0
	s_cmp_eq_u32 s99, 0
	s_cselect_b32 s100, 0x610, s100
	s_cselect_b32 s101, 0x8e0, s101
	s_cmp_eq_u32 s99, 1
	s_cselect_b32 s100, 0xb50, s100
	s_cselect_b32 s101, 0xe20, s101
	s_cmp_eq_u32 s99, 2
	s_cselect_b32 s100, 0x1090, s100
	s_cselect_b32 s101, 0x1360, s101
	s_add_i32 s98, s98, s100
	s_mov_b32 s99, s101
	s_cmp_ge_u32 s98, s99
	s_cbranch_scc1 .Lwqd_skip_A
	s_movk_i32 s100, 240
	s_mov_b32 s101, 1
	v_writelane_b32 v117, s0, 0
	v_writelane_b32 v117, s1, 1
	v_writelane_b32 v117, s2, 2
	v_writelane_b32 v117, s3, 3
	v_writelane_b32 v117, s4, 4
	v_writelane_b32 v117, s5, 5
	v_writelane_b32 v117, s6, 6
	v_writelane_b32 v117, s7, 7
	v_writelane_b32 v117, s8, 8
	v_writelane_b32 v117, s9, 9
	v_writelane_b32 v117, s10, 10
	v_writelane_b32 v117, s11, 11
	v_writelane_b32 v117, s12, 12
	v_writelane_b32 v117, s13, 13
	v_writelane_b32 v117, s14, 14
	v_writelane_b32 v117, s15, 15
	v_writelane_b32 v117, s16, 16
	v_writelane_b32 v117, s17, 17
	v_writelane_b32 v117, s18, 18
	v_writelane_b32 v117, s19, 19
	v_writelane_b32 v117, s20, 20
	v_writelane_b32 v117, s21, 21
	v_writelane_b32 v117, s22, 22
	v_writelane_b32 v117, s23, 23
	v_writelane_b32 v117, s24, 24
	v_writelane_b32 v117, s25, 25
	v_writelane_b32 v117, s26, 26
	v_writelane_b32 v117, s27, 27
	v_writelane_b32 v117, s28, 28
	v_writelane_b32 v117, s29, 29
	v_writelane_b32 v117, s30, 30
	v_writelane_b32 v117, s31, 31
	v_writelane_b32 v117, s32, 32
	v_writelane_b32 v117, s33, 33
	v_writelane_b32 v117, s34, 34
	v_writelane_b32 v117, s35, 35
	v_writelane_b32 v117, s36, 36
	v_writelane_b32 v117, s37, 37
	v_writelane_b32 v117, s38, 38
	v_writelane_b32 v117, s39, 39
	v_writelane_b32 v117, s40, 40
	v_writelane_b32 v117, s41, 41
	v_writelane_b32 v117, s42, 42
	v_writelane_b32 v117, s43, 43
	v_writelane_b32 v117, s44, 44
	v_writelane_b32 v117, s45, 45
	v_writelane_b32 v117, s46, 46
	v_writelane_b32 v117, s47, 47
	v_writelane_b32 v117, s48, 48
	v_writelane_b32 v117, s49, 49
	v_writelane_b32 v117, s50, 50
	v_writelane_b32 v117, s51, 51
	v_writelane_b32 v117, s52, 52
	v_writelane_b32 v117, s53, 53
	v_writelane_b32 v117, s54, 54
	v_writelane_b32 v117, s55, 55
	v_writelane_b32 v117, s56, 56
	v_writelane_b32 v117, s57, 57
	v_writelane_b32 v117, s58, 58
	v_writelane_b32 v117, s59, 59
	v_writelane_b32 v117, s60, 60
	v_writelane_b32 v117, s61, 61
	v_writelane_b32 v117, s62, 62
	v_writelane_b32 v117, s63, 63
	v_writelane_b32 v118, s64, 0
	v_writelane_b32 v118, s65, 1
	v_writelane_b32 v118, s66, 2
	v_writelane_b32 v118, s67, 3
	v_writelane_b32 v118, s68, 4
	v_writelane_b32 v118, s69, 5
	v_writelane_b32 v118, s70, 6
	v_writelane_b32 v118, s71, 7
	v_writelane_b32 v118, s72, 8
	v_writelane_b32 v118, s73, 9
	v_writelane_b32 v118, s74, 10
	v_writelane_b32 v118, s75, 11
	v_writelane_b32 v118, s76, 12
	v_writelane_b32 v118, s77, 13
	v_writelane_b32 v118, s78, 14
	v_writelane_b32 v118, s79, 15
	v_writelane_b32 v118, s80, 16
	v_writelane_b32 v118, s81, 17
	v_writelane_b32 v118, s82, 18
	v_writelane_b32 v118, s83, 19
	v_writelane_b32 v118, s84, 20
	v_writelane_b32 v118, s85, 21
	v_writelane_b32 v118, s86, 22
	v_writelane_b32 v118, s87, 23
	v_writelane_b32 v118, s88, 24
	v_writelane_b32 v118, s89, 25
	v_writelane_b32 v118, s90, 26
	v_writelane_b32 v118, s91, 27
	v_writelane_b32 v118, s92, 28
	v_writelane_b32 v118, s93, 29
	v_writelane_b32 v118, s94, 30
	v_writelane_b32 v118, s95, 31
	v_writelane_b32 v118, s96, 32
	v_writelane_b32 v118, s97, 33
	v_mov_b32_e32 v100, v0
	v_mov_b32_e32 v101, v50
	v_mov_b32_e32 v102, v51
	v_mov_b32_e32 v103, v52
	v_mov_b32_e32 v104, v54
	v_mov_b32_e32 v105, v55
	v_mov_b32_e32 v106, v56
	v_mov_b32_e32 v107, v58
	v_mov_b32_e32 v108, v59
	v_mov_b32_e32 v109, v60
	v_mov_b32_e32 v110, v62
	v_mov_b32_e32 v111, v63
	v_mov_b32_e32 v112, v64
	v_mov_b32_e32 v113, v67
	v_mov_b32_e32 v114, v75
	v_mov_b32_e32 v115, v77
	s_branch .Lwqd_entry
